# prep phase: the 512 key-block-mean items dealt wave-major over all 256 workgroups instead of 8 per workgroup on the first 64
# baseline (speedup 1.0000x reference)
; __device__ __forceinline__ void prep_phase(const Frame& F, const bf16_t* __restrict__ PROJ, const float* __restrict__ qn, const float* __restrict__ kvn, const f32x2* __restrict__ CS, bf16_t* __restrict__ CQN, bf16_t* __restrict__ CKVN, bf16_t* __restrict__ KB, float* __restrict__ KM) {
;     ...
;     for (int it = gw; it < NB * NBLK * HA; it += NGW) {
;         const int h = it % HA, blk = (it / HA) % NBLK, b = it / (HA * NBLK), c = lane & 7, r0 = lane >> 3;
;         const bf16_t* p = PROJ + ((size_t)b * SEQ + (size_t)blk * BLK + r0) * INCP + C_KA + h * 64 + c * 8;
.LBB0_336:
	s_lshr_b32 s6, s82, 3
	s_and_b32 s7, s96, 7
	s_mul_i32 s6, s6, s7
	s_lshr_b32 s7, s96, 3
	s_add_i32 s29, s6, s7
	s_cmpk_gt_i32 s29, 0x1ff
	s_cbranch_scc1 .LBB0_343
	v_mbcnt_lo_u32_b32 v1, -1, 0
	v_mbcnt_hi_u32_b32 v4, -1, v1
	v_and_b32_e32 v6, 64, v4
	v_xor_b32_e32 v1, 8, v4
	v_add_u32_e32 v6, 64, v6
	v_cmp_lt_i32_e32 vcc, v1, v6
	v_xor_b32_e32 v7, 16, v4
	v_ashrrev_i32_e32 v2, 3, v30
	v_cndmask_b32_e32 v1, v4, v1, vcc
	v_cmp_lt_i32_e32 vcc, v7, v6
	v_and_b32_e32 v8, 56, v32
	v_mov_b32_e32 v5, 0
	v_cndmask_b32_e32 v7, v4, v7, vcc
	v_lshlrev_b32_e32 v24, 2, v7
	v_xor_b32_e32 v7, 32, v4
	v_cmp_lt_i32_e32 vcc, v7, v6
	v_ashrrev_i32_e32 v3, 31, v2
	v_lshlrev_b32_e32 v1, 2, v1
	v_cndmask_b32_e32 v4, v4, v7, vcc
	v_lshlrev_b32_e32 v25, 2, v4
	v_and_b32_e32 v4, 7, v30
	v_lshlrev_b32_e32 v4, 4, v4
	v_cmp_gt_i32_e64 s[0:1], 8, v30
	v_lshl_add_u64 v[6:7], s[90:91], 0, v[4:5]
	s_movk_i32 s7, 0x2200
	s_mov_b32 s14, 0x3b351000
	s_mov_b32 s15, 0x3b362000
	s_mov_b32 s16, 0x3b373000
	s_mov_b32 s17, 0x3b384000
	s_mov_b32 s18, 0x3b395000
	s_mov_b32 s19, 0x3b3a6000
	s_mov_b32 s20, 0x3b3b7000
	s_mov_b32 s21, 0x3b3c8000
	s_mov_b32 s22, 0x3b3d9000
	s_mov_b32 s23, 0x3b3ea000
	s_mov_b32 s24, 0x3b3fb000
	s_mov_b32 s25, 0x3b40c000
	s_mov_b32 s26, 0x3b41d000
	s_mov_b32 s27, 0x3b42e000
	s_mov_b32 s28, 0x3b43f000
	v_lshlrev_b32_e32 v4, 2, v8
	s_mov_b32 s6, 0x3b800000
	s_branch .LBB0_339

; __device__ __forceinline__ void prep_phase(const Frame& F, const bf16_t* __restrict__ PROJ, const float* __restrict__ qn, const float* __restrict__ kvn, const f32x2* __restrict__ CS, bf16_t* __restrict__ CQN, bf16_t* __restrict__ CKVN, bf16_t* __restrict__ KB, float* __restrict__ KM) {
;     ...
;     for (int it = gw; it < NB * NBLK * HA; it += NGW) {
;         const int h = it % HA, blk = (it / HA) % NBLK, b = it / (HA * NBLK), c = lane & 7, r0 = lane >> 3;
;         const bf16_t* p = PROJ + ((size_t)b * SEQ + (size_t)blk * BLK + r0) * INCP + C_KA + h * 64 + c * 8;
.LBB0_2795:
	s_lshr_b32 s4, s82, 3
	s_and_b32 s5, s96, 7
	s_mul_i32 s4, s4, s5
	s_lshr_b32 s5, s96, 3
	s_add_i32 s12, s4, s5
	s_cmpk_gt_i32 s12, 0x1ff
	s_cbranch_scc1 .LBB0_2802
	v_mbcnt_lo_u32_b32 v1, -1, 0
	v_mbcnt_hi_u32_b32 v4, -1, v1
	v_and_b32_e32 v6, 64, v4
	v_xor_b32_e32 v1, 8, v4
	v_add_u32_e32 v6, 64, v6
	v_cmp_lt_i32_e32 vcc, v1, v6
	v_xor_b32_e32 v7, 16, v4
	v_ashrrev_i32_e32 v2, 3, v30
	v_cndmask_b32_e32 v1, v4, v1, vcc
	v_cmp_lt_i32_e32 vcc, v7, v6
	v_and_b32_e32 v8, 56, v32
	v_mov_b32_e32 v5, 0
	v_cndmask_b32_e32 v7, v4, v7, vcc
	v_lshlrev_b32_e32 v24, 2, v7
	v_xor_b32_e32 v7, 32, v4
	v_cmp_lt_i32_e32 vcc, v7, v6
	v_ashrrev_i32_e32 v3, 31, v2
	v_lshlrev_b32_e32 v1, 2, v1
	v_cndmask_b32_e32 v4, v4, v7, vcc
	v_lshlrev_b32_e32 v25, 2, v4
	v_and_b32_e32 v4, 7, v30
	v_lshlrev_b32_e32 v4, 4, v4
	v_cmp_gt_i32_e64 s[0:1], 8, v30
	v_lshl_add_u64 v[6:7], s[90:91], 0, v[4:5]
	s_movk_i32 s5, 0x2200
	v_lshlrev_b32_e32 v4, 2, v8
	s_mov_b32 s4, 0x3b800000
	s_branch .LBB0_2798
